# v66 + in-projection: tiles of the last (mostly padding) column block run a K-loop copy without the MFMAs and B-fragment reads of their unused upper 128 columns
# baseline (speedup 1.0000x reference)
.LBB0_2005:
	s_ashr_i32 s47, s46, 31
	s_lshl_b64 s[52:53], s[46:47], 19
	v_readlane_b32 s40, v253, 34
	v_readlane_b32 s41, v253, 35
	s_add_u32 s52, s40, s52
	s_addc_u32 s53, s41, s53
	s_and_b64 s[56:57], s[54:55], exec
	s_cselect_b32 s29, s53, s37
	s_cselect_b32 s47, s52, s36
	s_ashr_i32 s49, s48, 31
	s_lshl_b64 s[56:57], s[48:49], 19
	s_add_u32 s56, s35, s56
	s_addc_u32 s57, s64, s57
	s_and_b64 s[62:63], s[54:55], exec
	s_cselect_b32 s49, s57, s61
	s_cselect_b32 s59, s56, s60
	s_add_u32 s36, s36, 0x40080
	s_addc_u32 s37, s37, 0
	s_add_u32 s80, s60, 0x100
	v_mov_b32_e32 v2, 0
	s_addc_u32 s95, s61, 0
	s_mov_b32 vcc_lo, -2
	v_mov_b32_e32 v3, v2
	v_mov_b32_e32 v4, v2
	v_mov_b32_e32 v5, v2
	v_mov_b32_e32 v6, v2
	v_mov_b32_e32 v7, v2
	v_mov_b32_e32 v8, v2
	v_mov_b32_e32 v9, v2
	v_mov_b32_e32 v10, v2
	v_mov_b32_e32 v11, v2
	v_mov_b32_e32 v12, v2
	v_mov_b32_e32 v13, v2
	v_mov_b32_e32 v18, v2
	v_mov_b32_e32 v19, v2
	v_mov_b32_e32 v20, v2
	v_mov_b32_e32 v21, v2
	v_mov_b32_e32 v26, v2
	v_mov_b32_e32 v27, v2
	v_mov_b32_e32 v28, v2
	v_mov_b32_e32 v29, v2
	v_mov_b32_e32 v34, v2
	v_mov_b32_e32 v35, v2
	v_mov_b32_e32 v36, v2
	v_mov_b32_e32 v37, v2
	v_mov_b32_e32 v42, v2
	v_mov_b32_e32 v43, v2
	v_mov_b32_e32 v44, v2
	v_mov_b32_e32 v45, v2
	v_mov_b32_e32 v50, v2
	v_mov_b32_e32 v51, v2
	v_mov_b32_e32 v52, v2
	v_mov_b32_e32 v53, v2
	v_mov_b32_e32 v14, v2
	v_mov_b32_e32 v15, v2
	v_mov_b32_e32 v16, v2
	v_mov_b32_e32 v17, v2
	v_mov_b32_e32 v22, v2
	v_mov_b32_e32 v23, v2
	v_mov_b32_e32 v24, v2
	v_mov_b32_e32 v25, v2
	v_mov_b32_e32 v30, v2
	v_mov_b32_e32 v31, v2
	v_mov_b32_e32 v32, v2
	v_mov_b32_e32 v33, v2
	v_mov_b32_e32 v38, v2
	v_mov_b32_e32 v39, v2
	v_mov_b32_e32 v40, v2
	v_mov_b32_e32 v41, v2
	v_mov_b32_e32 v46, v2
	v_mov_b32_e32 v47, v2
	v_mov_b32_e32 v48, v2
	v_mov_b32_e32 v49, v2
	v_mov_b32_e32 v54, v2
	v_mov_b32_e32 v55, v2
	v_mov_b32_e32 v56, v2
	v_mov_b32_e32 v57, v2
	v_mov_b32_e32 v58, v2
	v_mov_b32_e32 v59, v2
	v_mov_b32_e32 v60, v2
	v_mov_b32_e32 v61, v2
	v_mov_b32_e32 v62, v2
	v_mov_b32_e32 v63, v2
	v_mov_b32_e32 v64, v2
	v_mov_b32_e32 v65, v2
	v_mov_b32_e32 v66, v2
	v_mov_b32_e32 v67, v2
	v_mov_b32_e32 v68, v2
	v_mov_b32_e32 v69, v2
	v_mov_b32_e32 v70, v2
	v_mov_b32_e32 v71, v2
	v_mov_b32_e32 v72, v2
	v_mov_b32_e32 v73, v2
	v_mov_b32_e32 v78, v2
	v_mov_b32_e32 v79, v2
	v_mov_b32_e32 v80, v2
	v_mov_b32_e32 v81, v2
	v_mov_b32_e32 v86, v2
	v_mov_b32_e32 v87, v2
	v_mov_b32_e32 v88, v2
	v_mov_b32_e32 v89, v2
	v_mov_b32_e32 v94, v2
	v_mov_b32_e32 v95, v2
	v_mov_b32_e32 v96, v2
	v_mov_b32_e32 v97, v2
	v_mov_b32_e32 v102, v2
	v_mov_b32_e32 v103, v2
	v_mov_b32_e32 v104, v2
	v_mov_b32_e32 v105, v2
	v_mov_b32_e32 v110, v2
	v_mov_b32_e32 v111, v2
	v_mov_b32_e32 v112, v2
	v_mov_b32_e32 v113, v2
	v_mov_b32_e32 v118, v2
	v_mov_b32_e32 v119, v2
	v_mov_b32_e32 v120, v2
	v_mov_b32_e32 v121, v2
	v_mov_b32_e32 v74, v2
	v_mov_b32_e32 v75, v2
	v_mov_b32_e32 v76, v2
	v_mov_b32_e32 v77, v2
	v_mov_b32_e32 v82, v2
	v_mov_b32_e32 v83, v2
	v_mov_b32_e32 v84, v2
	v_mov_b32_e32 v85, v2
	v_mov_b32_e32 v90, v2
	v_mov_b32_e32 v91, v2
	v_mov_b32_e32 v92, v2
	v_mov_b32_e32 v93, v2
	v_mov_b32_e32 v98, v2
	v_mov_b32_e32 v99, v2
	v_mov_b32_e32 v100, v2
	v_mov_b32_e32 v101, v2
	v_mov_b32_e32 v106, v2
	v_mov_b32_e32 v107, v2
	v_mov_b32_e32 v108, v2
	v_mov_b32_e32 v109, v2
	v_mov_b32_e32 v114, v2
	v_mov_b32_e32 v115, v2
	v_mov_b32_e32 v116, v2
	v_mov_b32_e32 v117, v2
	v_mov_b32_e32 v122, v2
	v_mov_b32_e32 v123, v2
	v_mov_b32_e32 v124, v2
	v_mov_b32_e32 v125, v2
	v_mov_b32_e32 v126, v2
	v_mov_b32_e32 v127, v2
	v_mov_b32_e32 v128, v2
	v_mov_b32_e32 v129, v2
	s_cmp_eq_u32 s50, 20
	s_cbranch_scc1 .Lkl_pn20
.LBB0_2006:
	v_or_b32_e32 v0, 0x10000, v164
	v_add_u32_e32 v165, 0x10400, v164
	ds_read_b128 v[158:161], v0
	ds_read_b128 v[166:169], v165
	v_add_u32_e32 v0, 0x10800, v164
	v_add_u32_e32 v165, 0x10c00, v164
	ds_read_b128 v[170:173], v0
	ds_read_b128 v[174:177], v165
	v_or_b32_e32 v0, 0x14000, v164
	v_add_u32_e32 v165, 0x14400, v164
	ds_read_b128 v[178:181], v0
	ds_read_b128 v[182:185], v165
	v_add_u32_e32 v0, 0x14800, v164
	v_add_u32_e32 v165, 0x14c00, v164
	ds_read_b128 v[186:189], v0
	ds_read_b128 v[190:193], v165
	s_add_u32 s40, s36, 0xfffc0080
	s_addc_u32 s41, s37, -1
	s_cmp_eq_u32 vcc_lo, 12
	s_cselect_b32 s63, s29, s41
	s_cselect_b32 s62, s47, s40
	s_cselect_b32 s61, s49, s95
	s_cselect_b32 s60, s59, s80
	v_lshl_add_u64 v[194:195], s[36:37], 0, v[138:139]
	s_add_i32 m0, s31, 0xc000
	ds_read_b128 v[200:203], v163
	ds_read_b128 v[204:207], v163 offset:1024
	ds_read_b128 v[208:211], v163 offset:2048
	ds_read_b128 v[212:215], v163 offset:3072
	ds_read_b128 v[216:219], v163 offset:4096
	ds_read_b128 v[220:223], v163 offset:5120
	ds_read_b128 v[236:239], v163 offset:6144
	ds_read_b128 v[240:243], v163 offset:7168
	global_load_lds_dwordx4 v[194:195], off
	v_lshl_add_u64 v[194:195], s[36:37], 0, v[140:141]
	s_add_i32 m0, s31, 0xe000
	s_nop 0
	global_load_lds_dwordx4 v[194:195], off
	s_waitcnt vmcnt(8)
	s_waitcnt lgkmcnt(0)
	s_barrier
	s_setprio 1
	s_waitcnt lgkmcnt(0)
	v_mfma_f32_16x16x32_bf16 v[126:129], v[158:161], v[200:203], v[126:129]
	v_mfma_f32_16x16x32_bf16 v[122:125], v[170:173], v[200:203], v[122:125]
	v_mfma_f32_16x16x32_bf16 v[114:117], v[158:161], v[208:211], v[114:117]
	v_mfma_f32_16x16x32_bf16 v[106:109], v[170:173], v[208:211], v[106:109]
	v_mfma_f32_16x16x32_bf16 v[98:101], v[158:161], v[216:219], v[98:101]
	v_mfma_f32_16x16x32_bf16 v[90:93], v[170:173], v[216:219], v[90:93]
	v_mfma_f32_16x16x32_bf16 v[82:85], v[158:161], v[236:239], v[82:85]
	v_mfma_f32_16x16x32_bf16 v[74:77], v[170:173], v[236:239], v[74:77]
	v_mfma_f32_16x16x32_bf16 v[126:129], v[166:169], v[204:207], v[126:129]
	v_mfma_f32_16x16x32_bf16 v[122:125], v[174:177], v[204:207], v[122:125]
	v_mfma_f32_16x16x32_bf16 v[114:117], v[166:169], v[212:215], v[114:117]
	v_mfma_f32_16x16x32_bf16 v[106:109], v[174:177], v[212:215], v[106:109]
	v_mfma_f32_16x16x32_bf16 v[98:101], v[166:169], v[220:223], v[98:101]
	v_mfma_f32_16x16x32_bf16 v[90:93], v[174:177], v[220:223], v[90:93]
	v_mfma_f32_16x16x32_bf16 v[82:85], v[166:169], v[240:243], v[82:85]
	v_mfma_f32_16x16x32_bf16 v[74:77], v[174:177], v[240:243], v[74:77]
	s_setprio 0
	s_setprio 1
	v_mfma_f32_16x16x32_bf16 v[118:121], v[178:181], v[200:203], v[118:121]
	v_mfma_f32_16x16x32_bf16 v[110:113], v[186:189], v[200:203], v[110:113]
	v_mfma_f32_16x16x32_bf16 v[102:105], v[178:181], v[208:211], v[102:105]
	v_mfma_f32_16x16x32_bf16 v[94:97], v[186:189], v[208:211], v[94:97]
	v_mfma_f32_16x16x32_bf16 v[86:89], v[178:181], v[216:219], v[86:89]
	v_mfma_f32_16x16x32_bf16 v[78:81], v[186:189], v[216:219], v[78:81]
	v_mfma_f32_16x16x32_bf16 v[70:73], v[178:181], v[236:239], v[70:73]
	v_mfma_f32_16x16x32_bf16 v[66:69], v[186:189], v[236:239], v[66:69]
	v_mfma_f32_16x16x32_bf16 v[118:121], v[182:185], v[204:207], v[118:121]
	v_mfma_f32_16x16x32_bf16 v[110:113], v[190:193], v[204:207], v[110:113]
	v_mfma_f32_16x16x32_bf16 v[102:105], v[182:185], v[212:215], v[102:105]
	v_mfma_f32_16x16x32_bf16 v[94:97], v[190:193], v[212:215], v[94:97]
	v_mfma_f32_16x16x32_bf16 v[86:89], v[182:185], v[220:223], v[86:89]
	v_mfma_f32_16x16x32_bf16 v[78:81], v[190:193], v[220:223], v[78:81]
	v_mfma_f32_16x16x32_bf16 v[70:73], v[182:185], v[240:243], v[70:73]
	v_mfma_f32_16x16x32_bf16 v[66:69], v[190:193], v[240:243], v[66:69]
	s_setprio 0
	s_barrier
	s_mov_b32 m0, s51
	v_lshl_add_u64 v[194:195], s[60:61], 0, v[132:133]
	s_add_u32 s40, s60, 0x40000
	ds_read_b128 v[200:203], v163 offset:16384
	ds_read_b128 v[204:207], v163 offset:17408
	ds_read_b128 v[208:211], v163 offset:18432
	ds_read_b128 v[212:215], v163 offset:19456
	ds_read_b128 v[216:219], v163 offset:20480
	ds_read_b128 v[220:223], v163 offset:21504
	ds_read_b128 v[236:239], v163 offset:22528
	ds_read_b128 v[240:243], v163 offset:23552
	global_load_lds_dwordx4 v[194:195], off
	v_lshl_add_u64 v[226:227], s[60:61], 0, v[136:137]
	s_mov_b32 m0, s65
	s_addc_u32 s41, s61, 0
	global_load_lds_dwordx4 v[226:227], off
	v_lshl_add_u64 v[244:245], s[40:41], 0, v[132:133]
	s_mov_b32 m0, s66
	v_lshl_add_u64 v[246:247], s[62:63], 0, v[134:135]
	global_load_lds_dwordx4 v[244:245], off
	v_lshl_add_u64 v[244:245], s[40:41], 0, v[136:137]
	s_mov_b32 m0, s67
	s_nop 0
	global_load_lds_dwordx4 v[244:245], off
	v_lshl_add_u64 v[244:245], s[62:63], 0, v[130:131]
	s_mov_b32 m0, s31
	s_nop 0
	global_load_lds_dwordx4 v[244:245], off
	s_mov_b32 m0, s82
	s_nop 0
	global_load_lds_dwordx4 v[246:247], off
	s_waitcnt vmcnt(8)
	s_waitcnt lgkmcnt(0)
	s_barrier
	s_setprio 1
	s_waitcnt lgkmcnt(0)
	v_mfma_f32_16x16x32_bf16 v[62:65], v[158:161], v[200:203], v[62:65]
	v_mfma_f32_16x16x32_bf16 v[58:61], v[170:173], v[200:203], v[58:61]
	v_mfma_f32_16x16x32_bf16 v[54:57], v[158:161], v[208:211], v[54:57]
	v_mfma_f32_16x16x32_bf16 v[46:49], v[170:173], v[208:211], v[46:49]
	v_mfma_f32_16x16x32_bf16 v[38:41], v[158:161], v[216:219], v[38:41]
	v_mfma_f32_16x16x32_bf16 v[30:33], v[170:173], v[216:219], v[30:33]
	v_mfma_f32_16x16x32_bf16 v[22:25], v[158:161], v[236:239], v[22:25]
	v_mfma_f32_16x16x32_bf16 v[14:17], v[170:173], v[236:239], v[14:17]
	v_mfma_f32_16x16x32_bf16 v[62:65], v[166:169], v[204:207], v[62:65]
	v_mfma_f32_16x16x32_bf16 v[58:61], v[174:177], v[204:207], v[58:61]
	v_mfma_f32_16x16x32_bf16 v[54:57], v[166:169], v[212:215], v[54:57]
	v_mfma_f32_16x16x32_bf16 v[46:49], v[174:177], v[212:215], v[46:49]
	v_mfma_f32_16x16x32_bf16 v[38:41], v[166:169], v[220:223], v[38:41]
	v_mfma_f32_16x16x32_bf16 v[30:33], v[174:177], v[220:223], v[30:33]
	v_mfma_f32_16x16x32_bf16 v[22:25], v[166:169], v[240:243], v[22:25]
	v_mfma_f32_16x16x32_bf16 v[14:17], v[174:177], v[240:243], v[14:17]
	s_setprio 0
	s_setprio 1
	v_mfma_f32_16x16x32_bf16 v[50:53], v[178:181], v[200:203], v[50:53]
	v_mfma_f32_16x16x32_bf16 v[42:45], v[186:189], v[200:203], v[42:45]
	v_mfma_f32_16x16x32_bf16 v[34:37], v[178:181], v[208:211], v[34:37]
	v_mfma_f32_16x16x32_bf16 v[26:29], v[186:189], v[208:211], v[26:29]
	v_mfma_f32_16x16x32_bf16 v[18:21], v[178:181], v[216:219], v[18:21]
	v_mfma_f32_16x16x32_bf16 v[10:13], v[186:189], v[216:219], v[10:13]
	v_mfma_f32_16x16x32_bf16 v[6:9], v[178:181], v[236:239], v[6:9]
	v_mfma_f32_16x16x32_bf16 v[2:5], v[186:189], v[236:239], v[2:5]
	v_mfma_f32_16x16x32_bf16 v[50:53], v[182:185], v[204:207], v[50:53]
	v_mfma_f32_16x16x32_bf16 v[42:45], v[190:193], v[204:207], v[42:45]
	v_mfma_f32_16x16x32_bf16 v[34:37], v[182:185], v[212:215], v[34:37]
	v_mfma_f32_16x16x32_bf16 v[26:29], v[190:193], v[212:215], v[26:29]
	v_mfma_f32_16x16x32_bf16 v[18:21], v[182:185], v[220:223], v[18:21]
	v_mfma_f32_16x16x32_bf16 v[10:13], v[190:193], v[220:223], v[10:13]
	v_mfma_f32_16x16x32_bf16 v[6:9], v[182:185], v[240:243], v[6:9]
	v_mfma_f32_16x16x32_bf16 v[2:5], v[190:193], v[240:243], v[2:5]
	s_setprio 0
	s_barrier
	v_or_b32_e32 v0, 0x18000, v164
	v_add_u32_e32 v165, 0x18400, v164
	ds_read_b128 v[158:161], v0
	ds_read_b128 v[166:169], v165
	v_add_u32_e32 v0, 0x18800, v164
	v_add_u32_e32 v165, 0x18c00, v164
	ds_read_b128 v[170:173], v0
	ds_read_b128 v[174:177], v165
	v_or_b32_e32 v0, 0x1c000, v164
	v_add_u32_e32 v165, 0x1c400, v164
	ds_read_b128 v[178:181], v0
	ds_read_b128 v[182:185], v165
	v_add_u32_e32 v0, 0x1c800, v164
	v_add_u32_e32 v165, 0x1cc00, v164
	ds_read_b128 v[186:189], v0
	ds_read_b128 v[190:193], v165
	s_add_u32 s40, s62, 0x40000
	s_addc_u32 s41, s63, 0
	s_mov_b32 m0, s83
	v_lshl_add_u64 v[248:249], s[40:41], 0, v[130:131]
	ds_read_b128 v[200:203], v163 offset:32768
	ds_read_b128 v[204:207], v163 offset:33792
	ds_read_b128 v[208:211], v163 offset:34816
	ds_read_b128 v[212:215], v163 offset:35840
	ds_read_b128 v[216:219], v163 offset:36864
	ds_read_b128 v[220:223], v163 offset:37888
	ds_read_b128 v[236:239], v163 offset:38912
	ds_read_b128 v[240:243], v163 offset:39936
	global_load_lds_dwordx4 v[248:249], off
	v_lshl_add_u64 v[248:249], s[40:41], 0, v[134:135]
	s_mov_b32 m0, s84
	s_nop 0
	global_load_lds_dwordx4 v[248:249], off
	s_waitcnt vmcnt(8)
	s_waitcnt lgkmcnt(0)
	s_barrier
	s_setprio 1
	s_waitcnt lgkmcnt(0)
	v_mfma_f32_16x16x32_bf16 v[126:129], v[158:161], v[200:203], v[126:129]
	v_mfma_f32_16x16x32_bf16 v[122:125], v[170:173], v[200:203], v[122:125]
	v_mfma_f32_16x16x32_bf16 v[114:117], v[158:161], v[208:211], v[114:117]
	v_mfma_f32_16x16x32_bf16 v[106:109], v[170:173], v[208:211], v[106:109]
	v_mfma_f32_16x16x32_bf16 v[98:101], v[158:161], v[216:219], v[98:101]
	v_mfma_f32_16x16x32_bf16 v[90:93], v[170:173], v[216:219], v[90:93]
	v_mfma_f32_16x16x32_bf16 v[82:85], v[158:161], v[236:239], v[82:85]
	v_mfma_f32_16x16x32_bf16 v[74:77], v[170:173], v[236:239], v[74:77]
	v_mfma_f32_16x16x32_bf16 v[126:129], v[166:169], v[204:207], v[126:129]
	v_mfma_f32_16x16x32_bf16 v[122:125], v[174:177], v[204:207], v[122:125]
	v_mfma_f32_16x16x32_bf16 v[114:117], v[166:169], v[212:215], v[114:117]
	v_mfma_f32_16x16x32_bf16 v[106:109], v[174:177], v[212:215], v[106:109]
	v_mfma_f32_16x16x32_bf16 v[98:101], v[166:169], v[220:223], v[98:101]
	v_mfma_f32_16x16x32_bf16 v[90:93], v[174:177], v[220:223], v[90:93]
	v_mfma_f32_16x16x32_bf16 v[82:85], v[166:169], v[240:243], v[82:85]
	v_mfma_f32_16x16x32_bf16 v[74:77], v[174:177], v[240:243], v[74:77]
	s_setprio 0
	s_setprio 1
	v_mfma_f32_16x16x32_bf16 v[118:121], v[178:181], v[200:203], v[118:121]
	v_mfma_f32_16x16x32_bf16 v[110:113], v[186:189], v[200:203], v[110:113]
	v_mfma_f32_16x16x32_bf16 v[102:105], v[178:181], v[208:211], v[102:105]
	v_mfma_f32_16x16x32_bf16 v[94:97], v[186:189], v[208:211], v[94:97]
	v_mfma_f32_16x16x32_bf16 v[86:89], v[178:181], v[216:219], v[86:89]
	v_mfma_f32_16x16x32_bf16 v[78:81], v[186:189], v[216:219], v[78:81]
	v_mfma_f32_16x16x32_bf16 v[70:73], v[178:181], v[236:239], v[70:73]
	v_mfma_f32_16x16x32_bf16 v[66:69], v[186:189], v[236:239], v[66:69]
	v_mfma_f32_16x16x32_bf16 v[118:121], v[182:185], v[204:207], v[118:121]
	v_mfma_f32_16x16x32_bf16 v[110:113], v[190:193], v[204:207], v[110:113]
	v_mfma_f32_16x16x32_bf16 v[102:105], v[182:185], v[212:215], v[102:105]
	v_mfma_f32_16x16x32_bf16 v[94:97], v[190:193], v[212:215], v[94:97]
	v_mfma_f32_16x16x32_bf16 v[86:89], v[182:185], v[220:223], v[86:89]
	v_mfma_f32_16x16x32_bf16 v[78:81], v[190:193], v[220:223], v[78:81]
	v_mfma_f32_16x16x32_bf16 v[70:73], v[182:185], v[240:243], v[70:73]
	v_mfma_f32_16x16x32_bf16 v[66:69], v[190:193], v[240:243], v[66:69]
	s_setprio 0
	s_barrier
	s_mov_b32 m0, s88
	v_lshl_add_u64 v[194:195], v[194:195], 0, s[18:19]
	s_add_u32 s40, s60, 0x40080
	ds_read_b128 v[200:203], v163 offset:49152
	ds_read_b128 v[204:207], v163 offset:50176
	ds_read_b128 v[208:211], v163 offset:51200
	ds_read_b128 v[212:215], v163 offset:52224
	ds_read_b128 v[216:219], v163 offset:53248
	ds_read_b128 v[220:223], v163 offset:54272
	ds_read_b128 v[236:239], v163 offset:55296
	ds_read_b128 v[240:243], v163 offset:56320
	global_load_lds_dwordx4 v[194:195], off
	v_lshl_add_u64 v[194:195], v[226:227], 0, s[18:19]
	s_mov_b32 m0, s89
	s_addc_u32 s41, s61, 0
	global_load_lds_dwordx4 v[194:195], off
	v_lshl_add_u64 v[194:195], s[40:41], 0, v[132:133]
	s_mov_b32 m0, s92
	s_nop 0
	global_load_lds_dwordx4 v[194:195], off
	v_lshl_add_u64 v[194:195], s[40:41], 0, v[136:137]
	s_mov_b32 m0, s93
	s_nop 0
	global_load_lds_dwordx4 v[194:195], off
	v_lshl_add_u64 v[194:195], v[244:245], 0, s[18:19]
	s_mov_b32 m0, s90
	s_nop 0
	global_load_lds_dwordx4 v[194:195], off
	v_lshl_add_u64 v[194:195], v[246:247], 0, s[18:19]
	s_mov_b32 m0, s91
	s_nop 0
	global_load_lds_dwordx4 v[194:195], off
	s_waitcnt vmcnt(8)
	s_waitcnt lgkmcnt(0)
	s_barrier
	s_setprio 1
	s_waitcnt lgkmcnt(0)
	v_mfma_f32_16x16x32_bf16 v[62:65], v[158:161], v[200:203], v[62:65]
	v_mfma_f32_16x16x32_bf16 v[58:61], v[170:173], v[200:203], v[58:61]
	v_mfma_f32_16x16x32_bf16 v[54:57], v[158:161], v[208:211], v[54:57]
	v_mfma_f32_16x16x32_bf16 v[46:49], v[170:173], v[208:211], v[46:49]
	v_mfma_f32_16x16x32_bf16 v[38:41], v[158:161], v[216:219], v[38:41]
	v_mfma_f32_16x16x32_bf16 v[30:33], v[170:173], v[216:219], v[30:33]
	v_mfma_f32_16x16x32_bf16 v[22:25], v[158:161], v[236:239], v[22:25]
	v_mfma_f32_16x16x32_bf16 v[14:17], v[170:173], v[236:239], v[14:17]
	v_mfma_f32_16x16x32_bf16 v[62:65], v[166:169], v[204:207], v[62:65]
	v_mfma_f32_16x16x32_bf16 v[58:61], v[174:177], v[204:207], v[58:61]
	v_mfma_f32_16x16x32_bf16 v[54:57], v[166:169], v[212:215], v[54:57]
	v_mfma_f32_16x16x32_bf16 v[46:49], v[174:177], v[212:215], v[46:49]
	v_mfma_f32_16x16x32_bf16 v[38:41], v[166:169], v[220:223], v[38:41]
	v_mfma_f32_16x16x32_bf16 v[30:33], v[174:177], v[220:223], v[30:33]
	v_mfma_f32_16x16x32_bf16 v[22:25], v[166:169], v[240:243], v[22:25]
	v_mfma_f32_16x16x32_bf16 v[14:17], v[174:177], v[240:243], v[14:17]
	s_setprio 0
	s_setprio 1
	v_mfma_f32_16x16x32_bf16 v[50:53], v[178:181], v[200:203], v[50:53]
	v_mfma_f32_16x16x32_bf16 v[42:45], v[186:189], v[200:203], v[42:45]
	v_mfma_f32_16x16x32_bf16 v[34:37], v[178:181], v[208:211], v[34:37]
	v_mfma_f32_16x16x32_bf16 v[26:29], v[186:189], v[208:211], v[26:29]
	v_mfma_f32_16x16x32_bf16 v[18:21], v[178:181], v[216:219], v[18:21]
	v_mfma_f32_16x16x32_bf16 v[10:13], v[186:189], v[216:219], v[10:13]
	v_mfma_f32_16x16x32_bf16 v[6:9], v[178:181], v[236:239], v[6:9]
	v_mfma_f32_16x16x32_bf16 v[2:5], v[186:189], v[236:239], v[2:5]
	v_mfma_f32_16x16x32_bf16 v[50:53], v[182:185], v[204:207], v[50:53]
	v_mfma_f32_16x16x32_bf16 v[42:45], v[190:193], v[204:207], v[42:45]
	v_mfma_f32_16x16x32_bf16 v[34:37], v[182:185], v[212:215], v[34:37]
	v_mfma_f32_16x16x32_bf16 v[26:29], v[190:193], v[212:215], v[26:29]
	v_mfma_f32_16x16x32_bf16 v[18:21], v[182:185], v[220:223], v[18:21]
	v_mfma_f32_16x16x32_bf16 v[10:13], v[190:193], v[220:223], v[10:13]
	v_mfma_f32_16x16x32_bf16 v[6:9], v[182:185], v[240:243], v[6:9]
	v_mfma_f32_16x16x32_bf16 v[2:5], v[190:193], v[240:243], v[2:5]
	s_setprio 0
	s_barrier
	s_add_i32 vcc_lo, vcc_lo, 2
	s_add_u32 s36, s36, 0x100
	s_addc_u32 s37, s37, 0
	s_add_u32 s80, s80, 0x100
	s_addc_u32 s95, s95, 0
	s_cmp_gt_u32 vcc_lo, 13
	s_cbranch_scc0 .LBB0_2006
	s_branch .Lkl_exit
.Lkl_pn20:
	v_or_b32_e32 v0, 0x10000, v164
	v_add_u32_e32 v165, 0x10400, v164
	ds_read_b128 v[158:161], v0
	ds_read_b128 v[166:169], v165
	v_add_u32_e32 v0, 0x10800, v164
	v_add_u32_e32 v165, 0x10c00, v164
	ds_read_b128 v[170:173], v0
	ds_read_b128 v[174:177], v165
	v_or_b32_e32 v0, 0x14000, v164
	v_add_u32_e32 v165, 0x14400, v164
	v_add_u32_e32 v0, 0x14800, v164
	v_add_u32_e32 v165, 0x14c00, v164
	s_add_u32 s40, s36, 0xfffc0080
	s_addc_u32 s41, s37, -1
	s_cmp_eq_u32 vcc_lo, 12
	s_cselect_b32 s63, s29, s41
	s_cselect_b32 s62, s47, s40
	s_cselect_b32 s61, s49, s95
	s_cselect_b32 s60, s59, s80
	v_lshl_add_u64 v[194:195], s[36:37], 0, v[138:139]
	s_add_i32 m0, s31, 0xc000
	ds_read_b128 v[200:203], v163
	ds_read_b128 v[204:207], v163 offset:1024
	ds_read_b128 v[208:211], v163 offset:2048
	ds_read_b128 v[212:215], v163 offset:3072
	ds_read_b128 v[216:219], v163 offset:4096
	ds_read_b128 v[220:223], v163 offset:5120
	ds_read_b128 v[236:239], v163 offset:6144
	ds_read_b128 v[240:243], v163 offset:7168
	global_load_lds_dwordx4 v[194:195], off
	v_lshl_add_u64 v[194:195], s[36:37], 0, v[140:141]
	s_add_i32 m0, s31, 0xe000
	s_nop 0
	global_load_lds_dwordx4 v[194:195], off
	s_waitcnt vmcnt(8)
	s_waitcnt lgkmcnt(0)
	s_barrier
	s_setprio 1
	s_waitcnt lgkmcnt(0)
	v_mfma_f32_16x16x32_bf16 v[126:129], v[158:161], v[200:203], v[126:129]
	v_mfma_f32_16x16x32_bf16 v[122:125], v[170:173], v[200:203], v[122:125]
	v_mfma_f32_16x16x32_bf16 v[114:117], v[158:161], v[208:211], v[114:117]
	v_mfma_f32_16x16x32_bf16 v[106:109], v[170:173], v[208:211], v[106:109]
	v_mfma_f32_16x16x32_bf16 v[98:101], v[158:161], v[216:219], v[98:101]
	v_mfma_f32_16x16x32_bf16 v[90:93], v[170:173], v[216:219], v[90:93]
	v_mfma_f32_16x16x32_bf16 v[82:85], v[158:161], v[236:239], v[82:85]
	v_mfma_f32_16x16x32_bf16 v[74:77], v[170:173], v[236:239], v[74:77]
	v_mfma_f32_16x16x32_bf16 v[126:129], v[166:169], v[204:207], v[126:129]
	v_mfma_f32_16x16x32_bf16 v[122:125], v[174:177], v[204:207], v[122:125]
	v_mfma_f32_16x16x32_bf16 v[114:117], v[166:169], v[212:215], v[114:117]
	v_mfma_f32_16x16x32_bf16 v[106:109], v[174:177], v[212:215], v[106:109]
	v_mfma_f32_16x16x32_bf16 v[98:101], v[166:169], v[220:223], v[98:101]
	v_mfma_f32_16x16x32_bf16 v[90:93], v[174:177], v[220:223], v[90:93]
	v_mfma_f32_16x16x32_bf16 v[82:85], v[166:169], v[240:243], v[82:85]
	v_mfma_f32_16x16x32_bf16 v[74:77], v[174:177], v[240:243], v[74:77]
	s_setprio 0
	s_setprio 1
	s_setprio 0
	s_barrier
	s_mov_b32 m0, s51
	v_lshl_add_u64 v[194:195], s[60:61], 0, v[132:133]
	s_add_u32 s40, s60, 0x40000
	ds_read_b128 v[200:203], v163 offset:16384
	ds_read_b128 v[204:207], v163 offset:17408
	ds_read_b128 v[208:211], v163 offset:18432
	ds_read_b128 v[212:215], v163 offset:19456
	ds_read_b128 v[216:219], v163 offset:20480
	ds_read_b128 v[220:223], v163 offset:21504
	ds_read_b128 v[236:239], v163 offset:22528
	ds_read_b128 v[240:243], v163 offset:23552
	global_load_lds_dwordx4 v[194:195], off
	v_lshl_add_u64 v[226:227], s[60:61], 0, v[136:137]
	s_mov_b32 m0, s65
	s_addc_u32 s41, s61, 0
	global_load_lds_dwordx4 v[226:227], off
	v_lshl_add_u64 v[244:245], s[40:41], 0, v[132:133]
	s_mov_b32 m0, s66
	v_lshl_add_u64 v[246:247], s[62:63], 0, v[134:135]
	global_load_lds_dwordx4 v[244:245], off
	v_lshl_add_u64 v[244:245], s[40:41], 0, v[136:137]
	s_mov_b32 m0, s67
	s_nop 0
	global_load_lds_dwordx4 v[244:245], off
	v_lshl_add_u64 v[244:245], s[62:63], 0, v[130:131]
	s_mov_b32 m0, s31
	s_nop 0
	global_load_lds_dwordx4 v[244:245], off
	s_mov_b32 m0, s82
	s_nop 0
	global_load_lds_dwordx4 v[246:247], off
	s_waitcnt vmcnt(8)
	s_waitcnt lgkmcnt(0)
	s_barrier
	s_setprio 1
	s_waitcnt lgkmcnt(0)
	v_mfma_f32_16x16x32_bf16 v[62:65], v[158:161], v[200:203], v[62:65]
	v_mfma_f32_16x16x32_bf16 v[58:61], v[170:173], v[200:203], v[58:61]
	v_mfma_f32_16x16x32_bf16 v[54:57], v[158:161], v[208:211], v[54:57]
	v_mfma_f32_16x16x32_bf16 v[46:49], v[170:173], v[208:211], v[46:49]
	v_mfma_f32_16x16x32_bf16 v[38:41], v[158:161], v[216:219], v[38:41]
	v_mfma_f32_16x16x32_bf16 v[30:33], v[170:173], v[216:219], v[30:33]
	v_mfma_f32_16x16x32_bf16 v[22:25], v[158:161], v[236:239], v[22:25]
	v_mfma_f32_16x16x32_bf16 v[14:17], v[170:173], v[236:239], v[14:17]
	v_mfma_f32_16x16x32_bf16 v[62:65], v[166:169], v[204:207], v[62:65]
	v_mfma_f32_16x16x32_bf16 v[58:61], v[174:177], v[204:207], v[58:61]
	v_mfma_f32_16x16x32_bf16 v[54:57], v[166:169], v[212:215], v[54:57]
	v_mfma_f32_16x16x32_bf16 v[46:49], v[174:177], v[212:215], v[46:49]
	v_mfma_f32_16x16x32_bf16 v[38:41], v[166:169], v[220:223], v[38:41]
	v_mfma_f32_16x16x32_bf16 v[30:33], v[174:177], v[220:223], v[30:33]
	v_mfma_f32_16x16x32_bf16 v[22:25], v[166:169], v[240:243], v[22:25]
	v_mfma_f32_16x16x32_bf16 v[14:17], v[174:177], v[240:243], v[14:17]
	s_setprio 0
	s_setprio 1
	s_setprio 0
	s_barrier
	v_or_b32_e32 v0, 0x18000, v164
	v_add_u32_e32 v165, 0x18400, v164
	ds_read_b128 v[158:161], v0
	ds_read_b128 v[166:169], v165
	v_add_u32_e32 v0, 0x18800, v164
	v_add_u32_e32 v165, 0x18c00, v164
	ds_read_b128 v[170:173], v0
	ds_read_b128 v[174:177], v165
	v_or_b32_e32 v0, 0x1c000, v164
	v_add_u32_e32 v165, 0x1c400, v164
	v_add_u32_e32 v0, 0x1c800, v164
	v_add_u32_e32 v165, 0x1cc00, v164
	s_add_u32 s40, s62, 0x40000
	s_addc_u32 s41, s63, 0
	s_mov_b32 m0, s83
	v_lshl_add_u64 v[248:249], s[40:41], 0, v[130:131]
	ds_read_b128 v[200:203], v163 offset:32768
	ds_read_b128 v[204:207], v163 offset:33792
	ds_read_b128 v[208:211], v163 offset:34816
	ds_read_b128 v[212:215], v163 offset:35840
	ds_read_b128 v[216:219], v163 offset:36864
	ds_read_b128 v[220:223], v163 offset:37888
	ds_read_b128 v[236:239], v163 offset:38912
	ds_read_b128 v[240:243], v163 offset:39936
	global_load_lds_dwordx4 v[248:249], off
	v_lshl_add_u64 v[248:249], s[40:41], 0, v[134:135]
	s_mov_b32 m0, s84
	s_nop 0
	global_load_lds_dwordx4 v[248:249], off
	s_waitcnt vmcnt(8)
	s_waitcnt lgkmcnt(0)
	s_barrier
	s_setprio 1
	s_waitcnt lgkmcnt(0)
	v_mfma_f32_16x16x32_bf16 v[126:129], v[158:161], v[200:203], v[126:129]
	v_mfma_f32_16x16x32_bf16 v[122:125], v[170:173], v[200:203], v[122:125]
	v_mfma_f32_16x16x32_bf16 v[114:117], v[158:161], v[208:211], v[114:117]
	v_mfma_f32_16x16x32_bf16 v[106:109], v[170:173], v[208:211], v[106:109]
	v_mfma_f32_16x16x32_bf16 v[98:101], v[158:161], v[216:219], v[98:101]
	v_mfma_f32_16x16x32_bf16 v[90:93], v[170:173], v[216:219], v[90:93]
	v_mfma_f32_16x16x32_bf16 v[82:85], v[158:161], v[236:239], v[82:85]
	v_mfma_f32_16x16x32_bf16 v[74:77], v[170:173], v[236:239], v[74:77]
	v_mfma_f32_16x16x32_bf16 v[126:129], v[166:169], v[204:207], v[126:129]
	v_mfma_f32_16x16x32_bf16 v[122:125], v[174:177], v[204:207], v[122:125]
	v_mfma_f32_16x16x32_bf16 v[114:117], v[166:169], v[212:215], v[114:117]
	v_mfma_f32_16x16x32_bf16 v[106:109], v[174:177], v[212:215], v[106:109]
	v_mfma_f32_16x16x32_bf16 v[98:101], v[166:169], v[220:223], v[98:101]
	v_mfma_f32_16x16x32_bf16 v[90:93], v[174:177], v[220:223], v[90:93]
	v_mfma_f32_16x16x32_bf16 v[82:85], v[166:169], v[240:243], v[82:85]
	v_mfma_f32_16x16x32_bf16 v[74:77], v[174:177], v[240:243], v[74:77]
	s_setprio 0
	s_setprio 1
	s_setprio 0
	s_barrier
	s_mov_b32 m0, s88
	v_lshl_add_u64 v[194:195], v[194:195], 0, s[18:19]
	s_add_u32 s40, s60, 0x40080
	ds_read_b128 v[200:203], v163 offset:49152
	ds_read_b128 v[204:207], v163 offset:50176
	ds_read_b128 v[208:211], v163 offset:51200
	ds_read_b128 v[212:215], v163 offset:52224
	ds_read_b128 v[216:219], v163 offset:53248
	ds_read_b128 v[220:223], v163 offset:54272
	ds_read_b128 v[236:239], v163 offset:55296
	ds_read_b128 v[240:243], v163 offset:56320
	global_load_lds_dwordx4 v[194:195], off
	v_lshl_add_u64 v[194:195], v[226:227], 0, s[18:19]
	s_mov_b32 m0, s89
	s_addc_u32 s41, s61, 0
	global_load_lds_dwordx4 v[194:195], off
	v_lshl_add_u64 v[194:195], s[40:41], 0, v[132:133]
	s_mov_b32 m0, s92
	s_nop 0
	global_load_lds_dwordx4 v[194:195], off
	v_lshl_add_u64 v[194:195], s[40:41], 0, v[136:137]
	s_mov_b32 m0, s93
	s_nop 0
	global_load_lds_dwordx4 v[194:195], off
	v_lshl_add_u64 v[194:195], v[244:245], 0, s[18:19]
	s_mov_b32 m0, s90
	s_nop 0
	global_load_lds_dwordx4 v[194:195], off
	v_lshl_add_u64 v[194:195], v[246:247], 0, s[18:19]
	s_mov_b32 m0, s91
	s_nop 0
	global_load_lds_dwordx4 v[194:195], off
	s_waitcnt vmcnt(8)
	s_waitcnt lgkmcnt(0)
	s_barrier
	s_setprio 1
	s_waitcnt lgkmcnt(0)
	v_mfma_f32_16x16x32_bf16 v[62:65], v[158:161], v[200:203], v[62:65]
	v_mfma_f32_16x16x32_bf16 v[58:61], v[170:173], v[200:203], v[58:61]
	v_mfma_f32_16x16x32_bf16 v[54:57], v[158:161], v[208:211], v[54:57]
	v_mfma_f32_16x16x32_bf16 v[46:49], v[170:173], v[208:211], v[46:49]
	v_mfma_f32_16x16x32_bf16 v[38:41], v[158:161], v[216:219], v[38:41]
	v_mfma_f32_16x16x32_bf16 v[30:33], v[170:173], v[216:219], v[30:33]
	v_mfma_f32_16x16x32_bf16 v[22:25], v[158:161], v[236:239], v[22:25]
	v_mfma_f32_16x16x32_bf16 v[14:17], v[170:173], v[236:239], v[14:17]
	v_mfma_f32_16x16x32_bf16 v[62:65], v[166:169], v[204:207], v[62:65]
	v_mfma_f32_16x16x32_bf16 v[58:61], v[174:177], v[204:207], v[58:61]
	v_mfma_f32_16x16x32_bf16 v[54:57], v[166:169], v[212:215], v[54:57]
	v_mfma_f32_16x16x32_bf16 v[46:49], v[174:177], v[212:215], v[46:49]
	v_mfma_f32_16x16x32_bf16 v[38:41], v[166:169], v[220:223], v[38:41]
	v_mfma_f32_16x16x32_bf16 v[30:33], v[174:177], v[220:223], v[30:33]
	v_mfma_f32_16x16x32_bf16 v[22:25], v[166:169], v[240:243], v[22:25]
	v_mfma_f32_16x16x32_bf16 v[14:17], v[174:177], v[240:243], v[14:17]
	s_setprio 0
	s_setprio 1
	s_setprio 0
	s_barrier
	s_add_i32 vcc_lo, vcc_lo, 2
	s_add_u32 s36, s36, 0x100
	s_addc_u32 s37, s37, 0
	s_add_u32 s80, s80, 0x100
	s_addc_u32 s95, s95, 0
	s_cmp_gt_u32 vcc_lo, 13
	s_cbranch_scc0 .Lkl_pn20
.Lkl_exit:
	s_and_b64 vcc, exec, s[16:17]
	s_cbranch_vccz .LBB0_2009
	s_barrier
